# P6 U sweep now covers all 8 tokens of a combine group in one pass over the expert ranges (own descriptor builder), V sweeps stay 4 tokens
# speedup vs baseline: 1.0391x; 1.0071x over previous
.LBB0_936:
	s_or_b64 exec, exec, s[0:1]
	v_cmp_lt_i32_e32 vcc, -1, v35
	s_movk_i32 s0, 0xff00
	v_lshl_add_u32 v25, v25, 2, s85
	v_cndmask_b32_e64 v44, v211, -1, vcc
	v_cmp_lt_i32_e32 vcc, -1, v34
	v_bitop3_b32 v35, v44, v35, s0 bitop3:0x78
	v_sub_f32_e32 v44, v35, v35
	v_cndmask_b32_e64 v88, v211, -1, vcc
	v_cmp_lt_i32_e32 vcc, -1, v33
	v_bitop3_b32 v34, v88, v34, s0 bitop3:0x78
	v_mul_f32_e32 v44, 0x3fb8aa3b, v44
	v_cndmask_b32_e64 v88, v211, -1, vcc
	v_cmp_lt_i32_e32 vcc, -1, v32
	v_sub_f32_e32 v34, v34, v35
	v_bitop3_b32 v33, v88, v33, s0 bitop3:0x78
	v_cndmask_b32_e64 v88, v211, -1, vcc
	v_cmp_lt_i32_e32 vcc, -1, v30
	v_exp_f32_e32 v44, v44
	v_mul_f32_e32 v34, 0x3fb8aa3b, v34
	v_sub_f32_e32 v33, v33, v35
	v_bitop3_b32 v32, v88, v32, s0 bitop3:0x78
	v_cndmask_b32_e64 v89, v211, -1, vcc
	v_cmp_lt_i32_e32 vcc, -1, v28
	v_exp_f32_e32 v34, v34
	v_mul_f32_e32 v33, 0x3fb8aa3b, v33
	v_sub_f32_e32 v32, v32, v35
	v_bitop3_b32 v30, v89, v30, s0 bitop3:0x78
	v_cndmask_b32_e64 v89, v211, -1, vcc
	v_cmp_lt_i32_e32 vcc, -1, v26
	v_exp_f32_e32 v33, v33
	v_mul_f32_e32 v32, 0x3fb8aa3b, v32
	v_sub_f32_e32 v30, v30, v35
	v_bitop3_b32 v28, v89, v28, s0 bitop3:0x78
	v_cndmask_b32_e64 v89, v211, -1, vcc
	v_cmp_lt_i32_e32 vcc, -1, v23
	v_exp_f32_e32 v32, v32
	v_mul_f32_e32 v30, 0x3fb8aa3b, v30
	v_sub_f32_e32 v28, v28, v35
	v_bitop3_b32 v26, v89, v26, s0 bitop3:0x78
	v_cndmask_b32_e64 v89, v211, -1, vcc
	v_cmp_lt_i32_e32 vcc, -1, v22
	v_add_f32_e32 v88, 0, v44
	v_exp_f32_e32 v30, v30
	v_mul_f32_e32 v28, 0x3fb8aa3b, v28
	v_sub_f32_e32 v26, v26, v35
	v_bitop3_b32 v23, v89, v23, s0 bitop3:0x78
	v_cndmask_b32_e64 v89, v211, -1, vcc
	v_cmp_lt_i32_e32 vcc, -1, v20
	v_add_f32_e32 v88, v88, v34
	v_exp_f32_e32 v28, v28
	v_mul_f32_e32 v26, 0x3fb8aa3b, v26
	v_sub_f32_e32 v23, v23, v35
	v_bitop3_b32 v22, v89, v22, s0 bitop3:0x78
	v_cndmask_b32_e64 v89, v211, -1, vcc
	v_cmp_lt_i32_e32 vcc, -1, v18
	v_add_f32_e32 v88, v88, v33
	v_exp_f32_e32 v26, v26
	v_mul_f32_e32 v23, 0x3fb8aa3b, v23
	v_sub_f32_e32 v22, v22, v35
	v_bitop3_b32 v20, v89, v20, s0 bitop3:0x78
	v_cndmask_b32_e64 v89, v211, -1, vcc
	v_cmp_lt_i32_e32 vcc, -1, v16
	v_add_f32_e32 v88, v88, v32
	v_exp_f32_e32 v23, v23
	v_mul_f32_e32 v22, 0x3fb8aa3b, v22
	v_sub_f32_e32 v20, v20, v35
	v_bitop3_b32 v18, v89, v18, s0 bitop3:0x78
	v_cndmask_b32_e64 v89, v211, -1, vcc
	v_cmp_lt_i32_e32 vcc, -1, v14
	v_add_f32_e32 v88, v88, v30
	v_exp_f32_e32 v22, v22
	v_mul_f32_e32 v20, 0x3fb8aa3b, v20
	v_sub_f32_e32 v18, v18, v35
	v_bitop3_b32 v16, v89, v16, s0 bitop3:0x78
	v_cndmask_b32_e64 v89, v211, -1, vcc
	v_cmp_lt_i32_e32 vcc, -1, v13
	v_add_f32_e32 v88, v88, v28
	v_exp_f32_e32 v20, v20
	v_mul_f32_e32 v18, 0x3fb8aa3b, v18
	v_sub_f32_e32 v16, v16, v35
	v_bitop3_b32 v14, v89, v14, s0 bitop3:0x78
	v_cndmask_b32_e64 v89, v211, -1, vcc
	v_cmp_lt_i32_e32 vcc, -1, v11
	v_add_f32_e32 v88, v88, v26
	v_exp_f32_e32 v18, v18
	v_mul_f32_e32 v16, 0x3fb8aa3b, v16
	v_sub_f32_e32 v14, v14, v35
	v_bitop3_b32 v13, v89, v13, s0 bitop3:0x78
	v_cndmask_b32_e64 v89, v211, -1, vcc
	v_cmp_lt_i32_e32 vcc, -1, v8
	v_add_f32_e32 v88, v88, v23
	v_exp_f32_e32 v16, v16
	v_mul_f32_e32 v14, 0x3fb8aa3b, v14
	v_sub_f32_e32 v13, v13, v35
	v_bitop3_b32 v11, v89, v11, s0 bitop3:0x78
	v_cndmask_b32_e64 v89, v211, -1, vcc
	v_add_f32_e32 v88, v88, v22
	v_exp_f32_e32 v14, v14
	v_mul_f32_e32 v13, 0x3fb8aa3b, v13
	v_sub_f32_e32 v11, v11, v35
	v_bitop3_b32 v8, v89, v8, s0 bitop3:0x78
	v_add_f32_e32 v88, v88, v20
	v_exp_f32_e32 v13, v13
	v_mul_f32_e32 v11, 0x3fb8aa3b, v11
	v_sub_f32_e32 v8, v8, v35
	v_add_f32_e32 v88, v88, v18
	v_exp_f32_e32 v11, v11
	v_mul_f32_e32 v8, 0x3fb8aa3b, v8
	v_add_f32_e32 v88, v88, v16
	v_exp_f32_e32 v8, v8
	v_add_f32_e32 v35, v88, v14
	v_add_f32_e32 v35, v35, v13
	v_add_f32_e32 v35, v35, v11
	v_add_f32_e32 v35, v35, v8
	v_div_scale_f32 v88, s[0:1], v35, v35, 1.0
	v_rcp_f32_e32 v89, v88
	s_waitcnt lgkmcnt(0)
	ds_write_b32 v25, v87 offset:4352
	ds_read_b32 v25, v86 offset:4352
	ds_add_rtn_u32 v86, v86, v0 offset:4608
	v_fma_f32 v90, -v88, v89, 1.0
	v_fmac_f32_e32 v89, v90, v89
	v_div_scale_f32 v90, vcc, 1.0, v35, 1.0
	v_mul_f32_e32 v91, v90, v89
	v_fma_f32 v92, -v88, v91, v90
	v_fmac_f32_e32 v91, v92, v89
	v_fma_f32 v88, -v88, v91, v90
	v_div_fmas_f32 v88, v88, v89, v91
	v_div_fixup_f32 v35, v88, v35, 1.0
	v_lshlrev_b32_e32 v1, 7, v1
	v_mul_f32_e32 v44, v44, v35
	s_waitcnt lgkmcnt(0)
	v_add3_u32 v25, v25, v1, v86
	s_waitcnt vmcnt(30)
	v_mul_f32_e32 v44, v68, v44
	v_lshl_add_u32 v25, v25, 2, s85
	ds_write_b32 v25, v44 offset:12288
	ds_write2st64_b32 v25, v66, v6 offset1:32
	ds_read_b32 v6, v85 offset:4352
	ds_add_rtn_u32 v25, v85, v0 offset:4608
	v_mul_f32_e32 v34, v34, v35
	s_waitcnt vmcnt(28)
	v_mul_f32_e32 v34, v67, v34
	s_mov_b32 s2, 0
	s_mov_b64 s[6:7], -1
	s_waitcnt lgkmcnt(0)
	v_add3_u32 v6, v6, v1, v25
	v_lshl_add_u32 v6, v6, 2, s85
	ds_write_b32 v6, v34 offset:12288
	ds_write2st64_b32 v6, v64, v5 offset1:32
	ds_read_b32 v5, v84 offset:4352
	ds_add_rtn_u32 v6, v84, v0 offset:4608
	v_mul_f32_e32 v25, v33, v35
	s_waitcnt vmcnt(26)
	v_mul_f32_e32 v25, v65, v25
	s_waitcnt lgkmcnt(0)
	v_add3_u32 v5, v5, v1, v6
	v_lshl_add_u32 v5, v5, 2, s85
	ds_write_b32 v5, v25 offset:12288
	ds_write2st64_b32 v5, v62, v4 offset1:32
	ds_read_b32 v4, v83 offset:4352
	ds_add_rtn_u32 v5, v83, v0 offset:4608
	v_mul_f32_e32 v6, v32, v35
	s_waitcnt vmcnt(24)
	v_mul_f32_e32 v6, v63, v6
	s_waitcnt lgkmcnt(0)
	v_add3_u32 v4, v4, v1, v5
	v_lshl_add_u32 v4, v4, 2, s85
	ds_write_b32 v4, v6 offset:12288
	ds_write2st64_b32 v4, v60, v2 offset1:32
	ds_read_b32 v2, v82 offset:4352
	ds_add_rtn_u32 v4, v82, v0 offset:4608
	v_mul_f32_e32 v5, v30, v35
	s_waitcnt vmcnt(22)
	v_mul_f32_e32 v5, v61, v5
	s_waitcnt lgkmcnt(0)
	v_add3_u32 v2, v2, v1, v4
	v_lshl_add_u32 v2, v2, 2, s85
	ds_write_b32 v2, v5 offset:12288
	ds_write2st64_b32 v2, v58, v12 offset1:32
	ds_read_b32 v2, v81 offset:4352
	ds_add_rtn_u32 v4, v81, v0 offset:4608
	v_mul_f32_e32 v5, v28, v35
	s_waitcnt vmcnt(20)
	v_mul_f32_e32 v5, v59, v5
	s_waitcnt lgkmcnt(0)
	v_add3_u32 v2, v2, v1, v4
	v_lshl_add_u32 v2, v2, 2, s85
	ds_write_b32 v2, v5 offset:12288
	ds_write2st64_b32 v2, v56, v10 offset1:32
	ds_read_b32 v2, v80 offset:4352
	ds_add_rtn_u32 v4, v80, v0 offset:4608
	v_mul_f32_e32 v5, v26, v35
	s_waitcnt vmcnt(18)
	v_mul_f32_e32 v5, v57, v5
	s_waitcnt lgkmcnt(0)
	v_add3_u32 v2, v2, v1, v4
	v_lshl_add_u32 v2, v2, 2, s85
	ds_write_b32 v2, v5 offset:12288
	ds_write2st64_b32 v2, v54, v9 offset1:32
	ds_read_b32 v2, v79 offset:4352
	ds_add_rtn_u32 v4, v79, v0 offset:4608
	v_mul_f32_e32 v5, v23, v35
	s_waitcnt vmcnt(16)
	v_mul_f32_e32 v5, v55, v5
	s_waitcnt lgkmcnt(0)
	v_add3_u32 v2, v2, v1, v4
	v_lshl_add_u32 v2, v2, 2, s85
	ds_write_b32 v2, v5 offset:12288
	ds_write2st64_b32 v2, v52, v7 offset1:32
	ds_read_b32 v2, v78 offset:4352
	ds_add_rtn_u32 v4, v78, v0 offset:4608
	v_mul_f32_e32 v5, v22, v35
	s_waitcnt vmcnt(14)
	v_mul_f32_e32 v5, v53, v5
	s_waitcnt lgkmcnt(0)
	v_add3_u32 v2, v2, v1, v4
	v_lshl_add_u32 v2, v2, 2, s85
	ds_write_b32 v2, v5 offset:12288
	ds_write2st64_b32 v2, v50, v21 offset1:32
	ds_read_b32 v2, v75 offset:4352
	ds_add_rtn_u32 v4, v75, v0 offset:4608
	v_mul_f32_e32 v5, v20, v35
	s_waitcnt vmcnt(12)
	v_mul_f32_e32 v5, v51, v5
	s_waitcnt lgkmcnt(0)
	v_add3_u32 v2, v2, v1, v4
	v_lshl_add_u32 v2, v2, 2, s85
	ds_write_b32 v2, v5 offset:12288
	ds_write2st64_b32 v2, v48, v19 offset1:32
	ds_read_b32 v2, v74 offset:4352
	ds_add_rtn_u32 v4, v74, v0 offset:4608
	v_mul_f32_e32 v5, v18, v35
	s_waitcnt vmcnt(10)
	v_mul_f32_e32 v5, v49, v5
	s_waitcnt lgkmcnt(0)
	v_add3_u32 v2, v2, v1, v4
	v_lshl_add_u32 v2, v2, 2, s85
	ds_write_b32 v2, v5 offset:12288
	ds_write2st64_b32 v2, v46, v17 offset1:32
	ds_read_b32 v2, v73 offset:4352
	ds_add_rtn_u32 v4, v73, v0 offset:4608
	v_mul_f32_e32 v5, v16, v35
	s_waitcnt vmcnt(8)
	v_mul_f32_e32 v5, v47, v5
	s_waitcnt lgkmcnt(0)
	v_add3_u32 v2, v2, v1, v4
	v_lshl_add_u32 v2, v2, 2, s85
	ds_write_b32 v2, v5 offset:12288
	ds_write2st64_b32 v2, v43, v15 offset1:32
	ds_read_b32 v2, v72 offset:4352
	ds_add_rtn_u32 v4, v72, v0 offset:4608
	v_mul_f32_e32 v5, v14, v35
	s_waitcnt vmcnt(6)
	v_mul_f32_e32 v5, v45, v5
	s_waitcnt lgkmcnt(0)
	v_add3_u32 v2, v2, v1, v4
	v_lshl_add_u32 v2, v2, 2, s85
	ds_write_b32 v2, v5 offset:12288
	ds_write2st64_b32 v2, v41, v31 offset1:32
	ds_read_b32 v2, v71 offset:4352
	ds_add_rtn_u32 v4, v71, v0 offset:4608
	v_mul_f32_e32 v5, v13, v35
	s_waitcnt vmcnt(4)
	v_mul_f32_e32 v5, v42, v5
	s_waitcnt lgkmcnt(0)
	v_add3_u32 v2, v2, v1, v4
	v_lshl_add_u32 v2, v2, 2, s85
	ds_write_b32 v2, v5 offset:12288
	ds_write2st64_b32 v2, v39, v29 offset1:32
	ds_read_b32 v2, v70 offset:4352
	ds_add_rtn_u32 v4, v70, v0 offset:4608
	v_mul_f32_e32 v5, v11, v35
	s_waitcnt vmcnt(2)
	v_mul_f32_e32 v5, v40, v5
	s_waitcnt lgkmcnt(0)
	v_add3_u32 v2, v2, v1, v4
	v_lshl_add_u32 v2, v2, 2, s85
	ds_write_b32 v2, v5 offset:12288
	ds_write2st64_b32 v2, v37, v27 offset1:32
	ds_read_b32 v2, v69 offset:4352
	ds_add_rtn_u32 v4, v69, v0 offset:4608
	v_mul_f32_e32 v5, v8, v35
	s_waitcnt vmcnt(0)
	v_mul_f32_e32 v5, v38, v5
	s_waitcnt lgkmcnt(0)
	v_add3_u32 v1, v2, v1, v4
	v_lshl_add_u32 v1, v1, 2, s85
	ds_write_b32 v1, v5 offset:12288
	ds_write2st64_b32 v1, v36, v24 offset1:32
	v_mov_b32_e32 v4, v179
	v_lshrrev_b32_e32 v5, 3, v4
	v_and_b32_e32 v6, 7, v4
	v_and_b32_e32 v7, 1, v5
	v_cmp_eq_u32_e32 vcc, 0, v7
	v_sub_u32_e32 v2, 7, v6
	s_nop 1
	v_cndmask_b32_e32 v6, v2, v6, vcc
	v_lshl_add_u32 v7, v6, 3, v5
	v_lshl_add_u32 v7, v7, 2, s85
	ds_read_b32 v8, v7 offset:4096
	ds_read_b32 v9, v7 offset:4352
	s_waitcnt lgkmcnt(0)
	v_add_u32_e32 v10, 7, v8
	v_lshrrev_b32_e32 v10, 3, v10
	v_mov_b32_e32 v11, v10
	v_subrev_u32_e32 v12, 1, v178
	v_max_i32_e32 v12, 0, v12
	v_cmp_le_u32_e32 vcc, 1, v178
	v_lshlrev_b32_e32 v12, 2, v12
	ds_bpermute_b32 v13, v12, v11
	s_waitcnt lgkmcnt(0)
	v_cndmask_b32_e32 v13, 0, v13, vcc
	v_add_u32_e32 v11, v11, v13
	v_subrev_u32_e32 v12, 2, v178
	v_max_i32_e32 v12, 0, v12
	v_cmp_le_u32_e32 vcc, 2, v178
	v_lshlrev_b32_e32 v12, 2, v12
	ds_bpermute_b32 v13, v12, v11
	s_waitcnt lgkmcnt(0)
	v_cndmask_b32_e32 v13, 0, v13, vcc
	v_add_u32_e32 v11, v11, v13
	v_subrev_u32_e32 v12, 4, v178
	v_max_i32_e32 v12, 0, v12
	v_cmp_le_u32_e32 vcc, 4, v178
	v_lshlrev_b32_e32 v12, 2, v12
	ds_bpermute_b32 v13, v12, v11
	s_waitcnt lgkmcnt(0)
	v_cndmask_b32_e32 v13, 0, v13, vcc
	v_add_u32_e32 v11, v11, v13
	v_subrev_u32_e32 v12, 8, v178
	v_max_i32_e32 v12, 0, v12
	v_cmp_le_u32_e32 vcc, 8, v178
	v_lshlrev_b32_e32 v12, 2, v12
	ds_bpermute_b32 v13, v12, v11
	s_waitcnt lgkmcnt(0)
	v_cndmask_b32_e32 v13, 0, v13, vcc
	v_add_u32_e32 v11, v11, v13
	v_subrev_u32_e32 v12, 16, v178
	v_max_i32_e32 v12, 0, v12
	v_cmp_le_u32_e32 vcc, 16, v178
	v_lshlrev_b32_e32 v12, 2, v12
	ds_bpermute_b32 v13, v12, v11
	s_waitcnt lgkmcnt(0)
	v_cndmask_b32_e32 v13, 0, v13, vcc
	v_add_u32_e32 v11, v11, v13
	v_subrev_u32_e32 v12, 32, v178
	v_max_i32_e32 v12, 0, v12
	v_cmp_le_u32_e32 vcc, 32, v178
	v_lshlrev_b32_e32 v12, 2, v12
	ds_bpermute_b32 v13, v12, v11
	s_waitcnt lgkmcnt(0)
	v_cndmask_b32_e32 v13, 0, v13, vcc
	v_add_u32_e32 v11, v11, v13
	v_sub_u32_e32 v12, v11, v10
	v_lshlrev_b32_e32 v13, 14, v6
	v_lshl_add_u32 v14, v6, 7, v9
	v_or_b32_e32 v13, v13, v14
	v_lshl_add_u32 v12, v12, 2, s85
	v_readlane_b32 s22, v11, 63
	s_mov_b64 s[14:15], exec
.Lp6_b8_loop:
	v_cmp_lt_i32_e32 vcc, 0, v8
	s_and_b64 exec, exec, vcc
	s_cbranch_execz .Lp6_b8_done
	v_min_i32_e32 v14, 8, v8
	v_lshl_or_b32 v14, v14, 10, v13
	ds_write_b32 v12, v14 offset:4864
	v_add_u32_e32 v13, 8, v13
	v_add_u32_e32 v12, 4, v12
	v_subrev_u32_e32 v8, 8, v8
	s_branch .Lp6_b8_loop
.Lp6_b8_done:
	s_mov_b64 exec, s[14:15]
	s_waitcnt vmcnt(0)
	v_mov_b32_e32 v1, s85
	ds_read_b32 v1, v1 offset:4864
	s_mov_b32 s0, s33
	s_ashr_i32 s1, s33, 31
	s_lshl_b64 s[0:1], s[0:1], 11
	s_waitcnt lgkmcnt(0)
	v_readfirstlane_b32 s26, v1
	v_lshl_add_u64 v[142:143], v[76:77], 0, s[0:1]
	s_lshr_b32 s2, s26, 3
	s_and_b32 s88, s2, 0x1ffff800
	v_lshl_add_u64 v[12:13], v[142:143], 0, s[88:89]
	global_load_dwordx4 v[8:11], v[12:13], off
	global_load_dwordx4 v[4:7], v[12:13], off offset:16
	s_and_b32 s2, s26, 0x3ff
	s_bfe_u32 s3, s26, 0x4000a
	v_cmp_gt_u32_e32 vcc, s3, v182
	s_lshl_b32 s2, s2, 2
	s_add_i32 s2, s2, s85
	v_cndmask_b32_e32 v1, 0, v182, vcc
	v_lshl_add_u32 v1, v1, 2, s2
	ds_read_b32 v1, v1 offset:8192
	s_waitcnt lgkmcnt(0)
	v_lshlrev_b32_e32 v1, 10, v1
	v_and_b32_e32 v1, 0x3fffc00, v1
	s_nop 0
	v_readlane_b32 s44, v1, 0
	v_readlane_b32 s45, v1, 1
	v_readlane_b32 s46, v1, 2
	v_readlane_b32 s47, v1, 3
	v_readlane_b32 s48, v1, 4
	v_readlane_b32 s49, v1, 5
	v_readlane_b32 s50, v1, 6
	v_readlane_b32 s51, v1, 7
	s_nop 4
	buffer_load_dwordx4 v[68:71], v181, s[8:11], s44 offen
	buffer_load_dwordx4 v[64:67], v181, s[8:11], s45 offen
	buffer_load_dwordx4 v[60:63], v181, s[8:11], s46 offen
	buffer_load_dwordx4 v[56:59], v181, s[8:11], s47 offen
	buffer_load_dwordx4 v[48:51], v181, s[8:11], s48 offen
	buffer_load_dwordx4 v[32:35], v181, s[8:11], s49 offen
	buffer_load_dwordx4 v[16:19], v181, s[8:11], s50 offen
	buffer_load_dwordx4 v[12:15], v181, s[8:11], s51 offen
	s_add_i32 s3, s22, -1
	s_min_i32 s2, s3, 1
	s_max_i32 s2, s2, 0
	s_lshl_b32 s2, s2, 2
	s_add_i32 s2, s85, s2
	v_mov_b32_e32 v1, s2
	ds_read_b32 v1, v1 offset:4864
	s_waitcnt lgkmcnt(0)
	v_readfirstlane_b32 s86, v1
	s_and_b32 s2, s86, 0x3ff
	s_bfe_u32 s3, s86, 0x4000a
	v_cmp_gt_u32_e32 vcc, s3, v182
	s_lshl_b32 s2, s2, 2
	s_add_i32 s2, s2, s85
	v_cndmask_b32_e32 v1, 0, v182, vcc
	v_lshl_add_u32 v1, v1, 2, s2
	ds_read_b32 v1, v1 offset:8192
	s_waitcnt lgkmcnt(0)
	v_lshlrev_b32_e32 v1, 10, v1
	v_and_b32_e32 v1, 0x3fffc00, v1
	s_nop 0
	v_readlane_b32 s44, v1, 0
	v_readlane_b32 s45, v1, 1
	v_readlane_b32 s46, v1, 2
	v_readlane_b32 s47, v1, 3
	v_readlane_b32 s48, v1, 4
	v_readlane_b32 s49, v1, 5
	v_readlane_b32 s50, v1, 6
	v_readlane_b32 s51, v1, 7
	s_nop 4
	buffer_load_dwordx4 v[72:75], v181, s[8:11], s44 offen
	buffer_load_dwordx4 v[52:55], v181, s[8:11], s45 offen
	buffer_load_dwordx4 v[44:47], v181, s[8:11], s46 offen
	buffer_load_dwordx4 v[40:43], v181, s[8:11], s47 offen
	buffer_load_dwordx4 v[36:39], v181, s[8:11], s48 offen
	buffer_load_dwordx4 v[28:31], v181, s[8:11], s49 offen
	buffer_load_dwordx4 v[24:27], v181, s[8:11], s50 offen
	buffer_load_dwordx4 v[20:23], v181, s[8:11], s51 offen
	s_add_i32 s3, s22, -1
	s_min_i32 s2, s3, 2
	s_max_i32 s2, s2, 0
	s_lshl_b32 s2, s2, 2
	s_add_i32 s2, s85, s2
	v_mov_b32_e32 v1, s2
	ds_read_b32 v1, v1 offset:4864
	s_waitcnt lgkmcnt(0)
	v_readfirstlane_b32 s27, v1
	s_and_b32 s2, s27, 0x3ff
	s_bfe_u32 s3, s27, 0x4000a
	v_cmp_gt_u32_e32 vcc, s3, v182
	s_lshl_b32 s2, s2, 2
	s_add_i32 s2, s2, s85
	v_cndmask_b32_e32 v1, 0, v182, vcc
	v_lshl_add_u32 v1, v1, 2, s2
	ds_read_b32 v1, v1 offset:8192
	s_waitcnt lgkmcnt(0)
	v_lshlrev_b32_e32 v1, 10, v1
	v_and_b32_e32 v1, 0x3fffc00, v1
	s_nop 0
	v_readlane_b32 s44, v1, 0
	v_readlane_b32 s45, v1, 1
	v_readlane_b32 s46, v1, 2
	v_readlane_b32 s47, v1, 3
	v_readlane_b32 s48, v1, 4
	v_readlane_b32 s49, v1, 5
	v_readlane_b32 s50, v1, 6
	v_readlane_b32 s51, v1, 7
	s_nop 4
	buffer_load_dwordx4 v[224:227], v181, s[8:11], s44 offen
	buffer_load_dwordx4 v[228:231], v181, s[8:11], s45 offen
	buffer_load_dwordx4 v[232:235], v181, s[8:11], s46 offen
	buffer_load_dwordx4 v[236:239], v181, s[8:11], s47 offen
	buffer_load_dwordx4 v[240:243], v181, s[8:11], s48 offen
	buffer_load_dwordx4 v[244:247], v181, s[8:11], s49 offen
	buffer_load_dwordx4 v[248:251], v181, s[8:11], s50 offen
	buffer_load_dwordx4 v[216:219], v181, s[8:11], s51 offen
	s_add_i32 s3, s22, -1
	s_min_i32 s2, s3, 3
	s_max_i32 s2, s2, 0
	s_lshl_b32 s2, s2, 2
	s_add_i32 s2, s85, s2
	v_mov_b32_e32 v1, s2
	ds_read_b32 v1, v1 offset:4864
	s_waitcnt lgkmcnt(0)
	v_readfirstlane_b32 s32, v1
	s_mov_b32 s23, 0
	s_mov_b64 s[0:1], -1

.Lp6_Adone:
	s_waitcnt vmcnt(0)
	s_mov_b32 s2, 0
	s_mov_b64 s[6:7], -1
	s_branch .LBB0_938

.LBB0_950:
	s_or_b64 exec, exec, s[0:1]
	s_waitcnt vmcnt(0)
	v_mov_b32_e32 v1, s85
	ds_read_b32 v1, v1 offset:4864
	s_or_b32 s96, s2, s33
	s_ashr_i32 s97, s96, 31
	v_readlane_b32 s22, v9, 63
	s_waitcnt lgkmcnt(0)
	v_readfirstlane_b32 s26, v1
	s_and_b32 s0, s26, 0x3ff
	s_bfe_u32 s1, s26, 0x4000a
	v_cmp_gt_u32_e32 vcc, s1, v182
	s_lshl_b32 s0, s0, 2
	s_add_i32 s0, s0, s85
	v_cndmask_b32_e32 v1, 0, v182, vcc
	v_lshl_add_u32 v1, v1, 2, s0
	ds_read_b32 v1, v1 offset:8192
	s_lshl_b64 s[0:1], s[96:97], 11
	s_lshr_b32 s23, s26, 3
	v_lshl_add_u64 v[142:143], v[76:77], 0, s[0:1]
	s_and_b32 s88, s23, 0x1ffff800
	s_waitcnt lgkmcnt(0)
	v_lshlrev_b32_e32 v1, 10, v1
	v_and_b32_e32 v1, 0x3fffc00, v1
	v_lshl_add_u64 v[12:13], v[142:143], 0, s[88:89]
	global_load_dwordx4 v[8:11], v[12:13], off
	global_load_dwordx4 v[4:7], v[12:13], off offset:16
	v_readlane_b32 s0, v1, 0
	v_readlane_b32 s1, v1, 1
	v_readlane_b32 s2, v1, 2
	v_readlane_b32 s3, v1, 3
	v_readlane_b32 s14, v1, 4
	v_readlane_b32 s15, v1, 5
	v_readlane_b32 s20, v1, 6
	v_readlane_b32 s21, v1, 7
	s_cmp_lt_i32 s22, 1
	s_cbranch_scc1 .LBB0_974
	v_mov_b32_e32 v84, 0
	s_mov_b32 s23, 0
	s_mov_b64 s[0:1], -1
	v_mov_b32_e32 v158, 0
	v_mov_b32_e32 v159, 0
	v_mov_b32_e32 v156, 0
	v_mov_b32_e32 v157, 0
	v_mov_b32_e32 v154, 0
	v_mov_b32_e32 v155, 0
	v_mov_b32_e32 v152, 0
	v_mov_b32_e32 v153, 0
	v_mov_b32_e32 v150, 0
	v_mov_b32_e32 v151, 0
	v_mov_b32_e32 v148, 0
	v_mov_b32_e32 v149, 0
	v_mov_b32_e32 v146, 0
	v_mov_b32_e32 v147, 0
	v_mov_b32_e32 v144, 0
	v_mov_b32_e32 v145, 0
	v_mov_b32_e32 v85, v84
	v_mov_b32_e32 v92, v84
	v_mov_b32_e32 v93, v84
	v_mov_b32_e32 v90, v84
	v_mov_b32_e32 v91, v84
	v_mov_b32_e32 v88, v84
	v_mov_b32_e32 v89, v84
	v_mov_b32_e32 v86, v84
	v_mov_b32_e32 v87, v84
	v_mov_b32_e32 v82, v84
	v_mov_b32_e32 v83, v84
	v_mov_b32_e32 v80, v84
	v_mov_b32_e32 v81, v84
	v_mov_b32_e32 v78, v84
	v_mov_b32_e32 v79, v84
	v_mov_b32_e32 v108, v84
	v_mov_b32_e32 v109, v84
	v_mov_b32_e32 v106, v84
	v_mov_b32_e32 v107, v84
	v_mov_b32_e32 v104, v84
	v_mov_b32_e32 v105, v84
	v_mov_b32_e32 v102, v84
	v_mov_b32_e32 v103, v84
	v_mov_b32_e32 v100, v84
	v_mov_b32_e32 v101, v84
	v_mov_b32_e32 v98, v84
	v_mov_b32_e32 v99, v84
	v_mov_b32_e32 v96, v84
	v_mov_b32_e32 v97, v84
	v_mov_b32_e32 v94, v84
	v_mov_b32_e32 v95, v84
	v_mov_b32_e32 v124, v84
	v_mov_b32_e32 v125, v84
	v_mov_b32_e32 v122, v84
	v_mov_b32_e32 v123, v84
	v_mov_b32_e32 v120, v84
	v_mov_b32_e32 v121, v84
	v_mov_b32_e32 v118, v84
	v_mov_b32_e32 v119, v84
	v_mov_b32_e32 v116, v84
	v_mov_b32_e32 v117, v84
	v_mov_b32_e32 v114, v84
	v_mov_b32_e32 v115, v84
	v_mov_b32_e32 v112, v84
	v_mov_b32_e32 v113, v84
	v_mov_b32_e32 v110, v84
	v_mov_b32_e32 v111, v84
	v_mov_b32_e32 v140, v84
	v_mov_b32_e32 v141, v84
	v_mov_b32_e32 v138, v84
	v_mov_b32_e32 v139, v84
	v_mov_b32_e32 v136, v84
	v_mov_b32_e32 v137, v84
	v_mov_b32_e32 v134, v84
	v_mov_b32_e32 v135, v84
	v_mov_b32_e32 v132, v84
	v_mov_b32_e32 v133, v84
	v_mov_b32_e32 v130, v84
	v_mov_b32_e32 v131, v84
	v_mov_b32_e32 v128, v84
	v_mov_b32_e32 v129, v84
	v_mov_b32_e32 v126, v84
	v_mov_b32_e32 v127, v84
	s_waitcnt vmcnt(0)
	s_add_i32 s3, s22, -1
	s_min_i32 s2, s3, 0
	s_max_i32 s2, s2, 0
	s_lshl_b32 s2, s2, 2
	s_add_i32 s2, s85, s2
	v_mov_b32_e32 v1, s2
	ds_read_b32 v1, v1 offset:4864
	s_waitcnt lgkmcnt(0)
	v_readfirstlane_b32 s26, v1
	s_and_b32 s2, s26, 0x3ff
	s_bfe_u32 s3, s26, 0x4000a
	v_cmp_gt_u32_e32 vcc, s3, v182
	s_lshl_b32 s2, s2, 2
	s_add_i32 s2, s2, s85
	v_cndmask_b32_e32 v1, 0, v182, vcc
	v_lshl_add_u32 v1, v1, 2, s2
	ds_read_b32 v1, v1 offset:8192
	s_waitcnt lgkmcnt(0)
	v_lshlrev_b32_e32 v1, 10, v1
	v_and_b32_e32 v1, 0x3fffc00, v1
	s_nop 0
	v_readlane_b32 s44, v1, 0
	v_readlane_b32 s45, v1, 1
	v_readlane_b32 s46, v1, 2
	v_readlane_b32 s47, v1, 3
	v_readlane_b32 s48, v1, 4
	v_readlane_b32 s49, v1, 5
	v_readlane_b32 s50, v1, 6
	v_readlane_b32 s51, v1, 7
	s_nop 4
	buffer_load_dwordx4 v[68:71], v181, s[92:95], s44 offen
	buffer_load_dwordx4 v[64:67], v181, s[92:95], s45 offen
	buffer_load_dwordx4 v[60:63], v181, s[92:95], s46 offen
	buffer_load_dwordx4 v[56:59], v181, s[92:95], s47 offen
	buffer_load_dwordx4 v[48:51], v181, s[92:95], s48 offen
	buffer_load_dwordx4 v[32:35], v181, s[92:95], s49 offen
	buffer_load_dwordx4 v[16:19], v181, s[92:95], s50 offen
	buffer_load_dwordx4 v[12:15], v181, s[92:95], s51 offen
	s_add_i32 s3, s22, -1
	s_min_i32 s2, s3, 1
	s_max_i32 s2, s2, 0
	s_lshl_b32 s2, s2, 2
	s_add_i32 s2, s85, s2
	v_mov_b32_e32 v1, s2
	ds_read_b32 v1, v1 offset:4864
	s_waitcnt lgkmcnt(0)
	v_readfirstlane_b32 s86, v1
	s_and_b32 s2, s86, 0x3ff
	s_bfe_u32 s3, s86, 0x4000a
	v_cmp_gt_u32_e32 vcc, s3, v182
	s_lshl_b32 s2, s2, 2
	s_add_i32 s2, s2, s85
	v_cndmask_b32_e32 v1, 0, v182, vcc
	v_lshl_add_u32 v1, v1, 2, s2
	ds_read_b32 v1, v1 offset:8192
	s_waitcnt lgkmcnt(0)
	v_lshlrev_b32_e32 v1, 10, v1
	v_and_b32_e32 v1, 0x3fffc00, v1
	s_nop 0
	v_readlane_b32 s44, v1, 0
	v_readlane_b32 s45, v1, 1
	v_readlane_b32 s46, v1, 2
	v_readlane_b32 s47, v1, 3
	v_readlane_b32 s48, v1, 4
	v_readlane_b32 s49, v1, 5
	v_readlane_b32 s50, v1, 6
	v_readlane_b32 s51, v1, 7
	s_nop 4
	buffer_load_dwordx4 v[72:75], v181, s[92:95], s44 offen
	buffer_load_dwordx4 v[52:55], v181, s[92:95], s45 offen
	buffer_load_dwordx4 v[44:47], v181, s[92:95], s46 offen
	buffer_load_dwordx4 v[40:43], v181, s[92:95], s47 offen
	buffer_load_dwordx4 v[36:39], v181, s[92:95], s48 offen
	buffer_load_dwordx4 v[28:31], v181, s[92:95], s49 offen
	buffer_load_dwordx4 v[24:27], v181, s[92:95], s50 offen
	buffer_load_dwordx4 v[20:23], v181, s[92:95], s51 offen
	s_add_i32 s3, s22, -1
	s_min_i32 s2, s3, 2
	s_max_i32 s2, s2, 0
	s_lshl_b32 s2, s2, 2
	s_add_i32 s2, s85, s2
	v_mov_b32_e32 v1, s2
	ds_read_b32 v1, v1 offset:4864
	s_waitcnt lgkmcnt(0)
	v_readfirstlane_b32 s27, v1
	s_and_b32 s2, s27, 0x3ff
	s_bfe_u32 s3, s27, 0x4000a
	v_cmp_gt_u32_e32 vcc, s3, v182
	s_lshl_b32 s2, s2, 2
	s_add_i32 s2, s2, s85
	v_cndmask_b32_e32 v1, 0, v182, vcc
	v_lshl_add_u32 v1, v1, 2, s2
	ds_read_b32 v1, v1 offset:8192
	s_waitcnt lgkmcnt(0)
	v_lshlrev_b32_e32 v1, 10, v1
	v_and_b32_e32 v1, 0x3fffc00, v1
	s_nop 0
	v_readlane_b32 s44, v1, 0
	v_readlane_b32 s45, v1, 1
	v_readlane_b32 s46, v1, 2
	v_readlane_b32 s47, v1, 3
	v_readlane_b32 s48, v1, 4
	v_readlane_b32 s49, v1, 5
	v_readlane_b32 s50, v1, 6
	v_readlane_b32 s51, v1, 7
	s_nop 4
	buffer_load_dwordx4 v[224:227], v181, s[92:95], s44 offen
	buffer_load_dwordx4 v[228:231], v181, s[92:95], s45 offen
	buffer_load_dwordx4 v[232:235], v181, s[92:95], s46 offen
	buffer_load_dwordx4 v[236:239], v181, s[92:95], s47 offen
	buffer_load_dwordx4 v[240:243], v181, s[92:95], s48 offen
	buffer_load_dwordx4 v[244:247], v181, s[92:95], s49 offen
	buffer_load_dwordx4 v[248:251], v181, s[92:95], s50 offen
	buffer_load_dwordx4 v[216:219], v181, s[92:95], s51 offen
	s_add_i32 s3, s22, -1
	s_min_i32 s2, s3, 3
	s_max_i32 s2, s2, 0
	s_lshl_b32 s2, s2, 2
	s_add_i32 s2, s85, s2
	v_mov_b32_e32 v1, s2
	ds_read_b32 v1, v1 offset:4864
	s_waitcnt lgkmcnt(0)
	v_readfirstlane_b32 s32, v1
	s_mov_b32 s23, 0
